# 96 phase-9 helpers + 64 phase-10 helpers + 40 proj helpers, contiguous deferred item range [6848, 58752); phase-3 order swap
# baseline (speedup 1.0000x reference)
;     ...
;         while (it < NIT) {
;             const int itB = it + NGW;
;             if (itB < NIT) { dB = decode(NIT - 1 - itB); tr_load(dB, vB); }
.LBB0_72:
	s_cmp_gt_i32 s42, 0xfcff
	s_cbranch_scc1 .LBB0_70
	s_add_i32 s44, s42, s48
	s_cmp_lt_i32 s44, 0x1ac0
	s_cbranch_scc1 .Lpt_1
	s_cmp_ge_i32 s44, 0xe580
	s_cbranch_scc1 .Lpt_1
	s_add_i32 s44, s44, 0xcac0

; #define LAS __attribute__((address_space(3)))
; #define GAS __attribute__((address_space(1)))
; #define LDS_WAIT() asm volatile("s_waitcnt lgkmcnt(0)" ::: "memory")
; __device__ __forceinline__ unsigned pk_fp8x4(float a, float b, float c, float d) { int p = __builtin_amdgcn_cvt_pk_fp8_f32(sat8(a), sat8(b), 0, false); p = __builtin_amdgcn_cvt_pk_fp8_f32(sat8(c), sat8(d), p, true); return (unsigned)p; }
; __device__ __forceinline__ void tr_finish(const TrDesc& d, f32x4 (&v)[16], LAS float* scr, int lane) {
;     const int kk = lane >> 4, q4 = lane & 15;
;     if (d.zero) {
; #pragma unroll
;         for (int i = 0; i < 16; ++i) v[i] = (f32x4){0.f, 0.f, 0.f, 0.f}; }
;     const int d0 = d.rope ? 8 * (q4 & 7) + (q4 >> 3) : 4 * q4, ds = d.rope ? 2 : 1;
;     { LAS float* rp = scr + kk * 65 + d0;
; #pragma unroll
;         for (int i = 0; i < 16; ++i) { rp[4 * i * 65] = v[i][0]; rp[4 * i * 65 + ds] = v[i][1]; rp[4 * i * 65 + 2 * ds] = v[i][2]; rp[4 * i * 65 + 3 * ds] = v[i][3]; } }
;     LDS_WAIT(); asm volatile("" ::: "memory");
;     if (d.f8) {
;         const int c = lane & 3, nl = lane >> 2; const LAS float* sp = scr + (16 * c) * 65 + nl; unsigned char* dp = d.dst + (size_t)nl * d.K + 16 * c;
; #pragma unroll
;         for (int j = 0; j < 4; ++j) { u32x4 o;
;             o.x = pk_fp8x4(sp[0 * 65 + 16 * j] * 32.0f, sp[1 * 65 + 16 * j] * 32.0f, sp[2 * 65 + 16 * j] * 32.0f, sp[3 * 65 + 16 * j] * 32.0f);
;             o.y = pk_fp8x4(sp[4 * 65 + 16 * j] * 32.0f, sp[5 * 65 + 16 * j] * 32.0f, sp[6 * 65 + 16 * j] * 32.0f, sp[7 * 65 + 16 * j] * 32.0f);
;             o.z = pk_fp8x4(sp[8 * 65 + 16 * j] * 32.0f, sp[9 * 65 + 16 * j] * 32.0f, sp[10 * 65 + 16 * j] * 32.0f, sp[11 * 65 + 16 * j] * 32.0f);
;             o.w = pk_fp8x4(sp[12 * 65 + 16 * j] * 32.0f, sp[13 * 65 + 16 * j] * 32.0f, sp[14 * 65 + 16 * j] * 32.0f, sp[15 * 65 + 16 * j] * 32.0f);
;             *(GAS u32x4*)(dp + (size_t)(16 * j) * d.K) = o; }
.LBB0_108:
	s_or_b64 exec, exec, s[22:23]
	s_cmp_eq_u32 s43, 0
	s_cselect_b64 vcc, -1, 0
	s_cmp_lg_u32 s43, 0
	s_cselect_b64 s[22:23], -1, 0
	v_cndmask_b32_e64 v2, 0, 1, s[22:23]
	s_and_b64 s[22:23], s[22:23], exec
	v_cndmask_b32_e32 v0, v140, v136, vcc
	s_cselect_b32 s0, 2, 1
	v_lshl_add_u32 v0, v0, 2, v141
	s_lshl_b32 s3, s0, 2
	v_add_u32_e32 v3, s3, v0
	v_lshlrev_b32_e64 v2, v2, 3
	s_waitcnt vmcnt(15)
	ds_write_b32 v3, v5
	v_lshl_add_u32 v3, s0, 3, v0
	v_lshl_add_u32 v2, v2, 2, v0
	v_subrev_u32_e32 v146, s3, v3
	ds_write_b32 v0, v4
	ds_write_b32 v3, v6
	ds_write_b32 v2, v7
	s_waitcnt vmcnt(14)
	ds_write_b32 v0, v8 offset:1040
	ds_write_b32 v146, v9 offset:1040
	ds_write_b32 v3, v10 offset:1040
	ds_write_b32 v2, v11 offset:1040
	s_waitcnt vmcnt(13)
	ds_write_b32 v0, v12 offset:2080
	ds_write_b32 v146, v13 offset:2080
	ds_write_b32 v3, v14 offset:2080
	ds_write_b32 v2, v15 offset:2080
	s_waitcnt vmcnt(12)
	ds_write_b32 v0, v16 offset:3120
	ds_write_b32 v146, v17 offset:3120
	ds_write_b32 v3, v18 offset:3120
	ds_write_b32 v2, v19 offset:3120
	s_waitcnt vmcnt(11)
	ds_write_b32 v0, v20 offset:4160
	ds_write_b32 v146, v21 offset:4160
	ds_write_b32 v3, v22 offset:4160
	ds_write_b32 v2, v23 offset:4160
	s_waitcnt vmcnt(10)
	ds_write_b32 v0, v24 offset:5200
	ds_write_b32 v146, v25 offset:5200
	ds_write_b32 v3, v26 offset:5200
	ds_write_b32 v2, v27 offset:5200
	s_waitcnt vmcnt(9)
	ds_write_b32 v0, v28 offset:6240
	ds_write_b32 v146, v29 offset:6240
	ds_write_b32 v3, v30 offset:6240
	ds_write_b32 v2, v31 offset:6240
	s_waitcnt vmcnt(8)
	ds_write_b32 v0, v32 offset:7280
	ds_write_b32 v146, v33 offset:7280
	ds_write_b32 v3, v34 offset:7280
	ds_write_b32 v2, v35 offset:7280
	s_waitcnt vmcnt(7)
	ds_write_b32 v0, v36 offset:8320
	ds_write_b32 v146, v37 offset:8320
	ds_write_b32 v3, v38 offset:8320
	ds_write_b32 v2, v39 offset:8320
	s_waitcnt vmcnt(6)
	ds_write_b32 v0, v40 offset:9360
	ds_write_b32 v146, v41 offset:9360
	ds_write_b32 v3, v42 offset:9360
	ds_write_b32 v2, v43 offset:9360
	s_waitcnt vmcnt(5)
	ds_write_b32 v0, v44 offset:10400
	ds_write_b32 v146, v45 offset:10400
	ds_write_b32 v3, v46 offset:10400
	ds_write_b32 v2, v47 offset:10400
	s_waitcnt vmcnt(4)
	ds_write_b32 v0, v48 offset:11440
	ds_write_b32 v146, v49 offset:11440
	ds_write_b32 v3, v50 offset:11440
	ds_write_b32 v2, v51 offset:11440
	s_waitcnt vmcnt(3)
	ds_write_b32 v0, v52 offset:12480
	ds_write_b32 v146, v53 offset:12480
	ds_write_b32 v3, v54 offset:12480
	ds_write_b32 v2, v55 offset:12480
	s_waitcnt vmcnt(2)
	ds_write_b32 v0, v56 offset:13520
	ds_write_b32 v146, v57 offset:13520
	ds_write_b32 v3, v58 offset:13520
	ds_write_b32 v2, v59 offset:13520
	s_waitcnt vmcnt(1)
	ds_write_b32 v0, v60 offset:14560
	ds_write_b32 v146, v61 offset:14560
	ds_write_b32 v3, v62 offset:14560
	ds_write_b32 v2, v63 offset:14560
	s_waitcnt vmcnt(0)
	ds_write_b32 v0, v64 offset:15600
	ds_write_b32 v146, v65 offset:15600
	ds_write_b32 v3, v66 offset:15600
	ds_write_b32 v2, v67 offset:15600
	s_waitcnt lgkmcnt(0)
	ds_read2_b32 v[2:3], v142 offset1:16
	ds_read2_b32 v[148:149], v142 offset0:65 offset1:81
	ds_read2_b32 v[154:155], v142 offset0:130 offset1:146
	ds_read2_b32 v[156:157], v142 offset0:195 offset1:211
	v_mov_b32_e32 v150, 0
	s_waitcnt lgkmcnt(3)
	v_mul_f32_e32 v0, 0x42000000, v2
	s_waitcnt lgkmcnt(2)
	v_mul_f32_e32 v2, 0x42000000, v148
	v_med3_f32 v0, v0, s41, v143
	s_waitcnt lgkmcnt(0)
	v_mul_f32_e32 v147, 0x42000000, v156
	v_med3_f32 v2, v2, s41, v143
	v_cvt_pk_fp8_f32 v150, v0, v2
	v_med3_f32 v2, v147, s41, v143
	v_add_u32_e32 v147, 0x400, v142
	ds_read2_b32 v[160:161], v147 offset0:4 offset1:20
	ds_read2_b32 v[162:163], v147 offset0:69 offset1:85
	ds_read2_b32 v[164:165], v147 offset0:134 offset1:150
	ds_read2_b32 v[166:167], v147 offset0:199 offset1:215
	v_mul_f32_e32 v146, 0x42000000, v154
	v_med3_f32 v0, v146, s41, v143
	v_cvt_pk_fp8_f32 v150, v0, v2 op_sel:[0,0,1]
	s_waitcnt lgkmcnt(3)
	v_mul_f32_e32 v0, 0x42000000, v160
	s_waitcnt lgkmcnt(2)
	v_mul_f32_e32 v2, 0x42000000, v162
	s_waitcnt lgkmcnt(0)
	v_mul_f32_e32 v148, 0x42000000, v166
	v_med3_f32 v0, v0, s41, v143
	v_med3_f32 v2, v2, s41, v143
	v_mov_b32_e32 v151, 0
	v_cvt_pk_fp8_f32 v151, v0, v2
	v_med3_f32 v2, v148, s41, v143
	v_add_u32_e32 v148, 0x800, v142
	ds_read2_b32 v[168:169], v148 offset0:8 offset1:24
	ds_read2_b32 v[170:171], v148 offset0:73 offset1:89
	ds_read2_b32 v[172:173], v148 offset0:138 offset1:154
	ds_read2_b32 v[174:175], v148 offset0:203 offset1:219
	v_mul_f32_e32 v146, 0x42000000, v164
	v_med3_f32 v0, v146, s41, v143
	v_cvt_pk_fp8_f32 v151, v0, v2 op_sel:[0,0,1]
	s_waitcnt lgkmcnt(3)
	v_mul_f32_e32 v0, 0x42000000, v168
	s_waitcnt lgkmcnt(2)
	v_mul_f32_e32 v2, 0x42000000, v170
	s_waitcnt lgkmcnt(1)
	v_mul_f32_e32 v146, 0x42000000, v172
	v_med3_f32 v0, v0, s41, v143
	v_med3_f32 v2, v2, s41, v143
	v_mov_b32_e32 v152, 0
	v_cvt_pk_fp8_f32 v152, v0, v2
	v_med3_f32 v0, v146, s41, v143
	v_add_u32_e32 v146, 0xc00, v142
	ds_read2_b32 v[176:177], v146 offset0:12 offset1:28
	ds_read2_b32 v[178:179], v146 offset0:77 offset1:93
	ds_read2_b32 v[180:181], v146 offset0:142 offset1:158
	s_waitcnt lgkmcnt(3)
	v_mul_f32_e32 v153, 0x42000000, v174
	v_med3_f32 v2, v153, s41, v143
	ds_read2_b32 v[182:183], v146 offset0:207 offset1:223
	v_cvt_pk_fp8_f32 v152, v0, v2 op_sel:[0,0,1]
	s_waitcnt lgkmcnt(3)
	v_mul_f32_e32 v0, 0x42000000, v176
	s_waitcnt lgkmcnt(2)
	v_mul_f32_e32 v2, 0x42000000, v178
	v_med3_f32 v0, v0, s41, v143
	v_med3_f32 v2, v2, s41, v143
	v_mov_b32_e32 v153, 0
	v_cvt_pk_fp8_f32 v153, v0, v2
	s_waitcnt lgkmcnt(1)
	v_mul_f32_e32 v154, 0x42000000, v180
	s_waitcnt lgkmcnt(0)
; #define GAS __attribute__((address_space(1)))
; __device__ __forceinline__ unsigned pk_fp8x4(float a, float b, float c, float d) { int p = __builtin_amdgcn_cvt_pk_fp8_f32(sat8(a), sat8(b), 0, false); p = __builtin_amdgcn_cvt_pk_fp8_f32(sat8(c), sat8(d), p, true); return (unsigned)p; }
; __device__ __forceinline__ void tr_finish(const TrDesc& d, f32x4 (&v)[16], LAS float* scr, int lane) {
;     ...
;         for (int j = 0; j < 4; ++j) { u32x4 o;
;             o.x = pk_fp8x4(sp[0 * 65 + 16 * j] * 32.0f, sp[1 * 65 + 16 * j] * 32.0f, sp[2 * 65 + 16 * j] * 32.0f, sp[3 * 65 + 16 * j] * 32.0f);
;             o.y = pk_fp8x4(sp[4 * 65 + 16 * j] * 32.0f, sp[5 * 65 + 16 * j] * 32.0f, sp[6 * 65 + 16 * j] * 32.0f, sp[7 * 65 + 16 * j] * 32.0f);
;             o.z = pk_fp8x4(sp[8 * 65 + 16 * j] * 32.0f, sp[9 * 65 + 16 * j] * 32.0f, sp[10 * 65 + 16 * j] * 32.0f, sp[11 * 65 + 16 * j] * 32.0f);
;             o.w = pk_fp8x4(sp[12 * 65 + 16 * j] * 32.0f, sp[13 * 65 + 16 * j] * 32.0f, sp[14 * 65 + 16 * j] * 32.0f, sp[15 * 65 + 16 * j] * 32.0f);
;             *(GAS u32x4*)(dp + (size_t)(16 * j) * d.K) = o; }
;     ...
;             if (itB >= NIT) break;
;             const int itA = itB + NGW;
;             if (itA < NIT) { dA = decode(NIT - 1 - itA); tr_load(dA, vA); }
	v_mul_f32_e32 v0, 0x42000000, v182
	v_med3_f32 v2, v154, s41, v143
	v_med3_f32 v0, v0, s41, v143
	v_cvt_pk_fp8_f32 v153, v2, v0 op_sel:[0,0,1]
	v_mov_b64_e32 v[158:159], s[16:17]
	v_mad_i64_i32 v[158:159], s[22:23], s2, v132, v[158:159]
	v_lshl_add_u64 v[158:159], v[158:159], 0, v[134:135]
	v_mul_f32_e32 v0, 0x42000000, v3
	v_mul_f32_e32 v2, 0x42000000, v149
	global_store_dwordx4 v[158:159], v[150:153], off
	v_med3_f32 v0, v0, s41, v143
	v_med3_f32 v2, v2, s41, v143
	v_mov_b32_e32 v150, 0
	v_cvt_pk_fp8_f32 v150, v0, v2
	v_mul_f32_e32 v3, 0x42000000, v155
	v_mul_f32_e32 v0, 0x42000000, v157
	v_med3_f32 v2, v3, s41, v143
	v_med3_f32 v0, v0, s41, v143
	v_cvt_pk_fp8_f32 v150, v2, v0 op_sel:[0,0,1]
	v_mul_f32_e32 v0, 0x42000000, v161
	v_mul_f32_e32 v2, 0x42000000, v163
	v_med3_f32 v0, v0, s41, v143
	v_med3_f32 v2, v2, s41, v143
	v_mov_b32_e32 v151, 0
	v_cvt_pk_fp8_f32 v151, v0, v2
	v_mul_f32_e32 v3, 0x42000000, v165
	v_mul_f32_e32 v0, 0x42000000, v167
	v_med3_f32 v2, v3, s41, v143
	v_med3_f32 v0, v0, s41, v143
	v_cvt_pk_fp8_f32 v151, v2, v0 op_sel:[0,0,1]
	v_mul_f32_e32 v0, 0x42000000, v169
	v_mul_f32_e32 v2, 0x42000000, v171
	v_med3_f32 v0, v0, s41, v143
	v_med3_f32 v2, v2, s41, v143
	v_mov_b32_e32 v152, 0
	v_cvt_pk_fp8_f32 v152, v0, v2
	v_mul_f32_e32 v3, 0x42000000, v173
	v_mul_f32_e32 v0, 0x42000000, v175
	v_med3_f32 v2, v3, s41, v143
	v_med3_f32 v0, v0, s41, v143
	v_cvt_pk_fp8_f32 v152, v2, v0 op_sel:[0,0,1]
	v_mul_f32_e32 v0, 0x42000000, v177
	v_mul_f32_e32 v2, 0x42000000, v179
	v_med3_f32 v0, v0, s41, v143
	v_med3_f32 v2, v2, s41, v143
	v_mov_b32_e32 v153, 0
	v_cvt_pk_fp8_f32 v153, v0, v2
	s_ashr_i32 s3, s2, 31
	v_mul_f32_e32 v3, 0x42000000, v181
	v_mul_f32_e32 v0, 0x42000000, v183
	v_med3_f32 v2, v3, s41, v143
	v_med3_f32 v0, v0, s41, v143
	s_lshl_b64 s[22:23], s[2:3], 4
	v_cvt_pk_fp8_f32 v153, v2, v0 op_sel:[0,0,1]
	v_lshl_add_u64 v[2:3], v[158:159], 0, s[22:23]
	ds_read2_b32 v[154:155], v142 offset0:32 offset1:48
	ds_read2_b32 v[156:157], v142 offset0:97 offset1:113
	ds_read2_b32 v[158:159], v142 offset0:162 offset1:178
	ds_read2_b32 v[160:161], v142 offset0:227 offset1:243
	s_andn2_b64 vcc, exec, s[20:21]
	s_waitcnt lgkmcnt(3)
	v_mul_f32_e32 v0, 0x42000000, v154
	s_waitcnt lgkmcnt(2)
	v_mul_f32_e32 v149, 0x42000000, v156
	global_store_dwordx4 v[2:3], v[150:153], off
	v_med3_f32 v0, v0, s41, v143
	v_med3_f32 v149, v149, s41, v143
	v_mov_b32_e32 v150, 0
	v_cvt_pk_fp8_f32 v150, v0, v149
	ds_read2_b32 v[162:163], v147 offset0:36 offset1:52
	ds_read2_b32 v[164:165], v147 offset0:101 offset1:117
	ds_read2_b32 v[166:167], v147 offset0:166 offset1:182
	ds_read2_b32 v[168:169], v147 offset0:231 offset1:247
	s_waitcnt lgkmcnt(5)
	v_mul_f32_e32 v151, 0x42000000, v158
	s_waitcnt lgkmcnt(4)
	v_mul_f32_e32 v152, 0x42000000, v160
	v_med3_f32 v0, v151, s41, v143
	v_med3_f32 v149, v152, s41, v143
	v_cvt_pk_fp8_f32 v150, v0, v149 op_sel:[0,0,1]
	s_waitcnt lgkmcnt(3)
	v_mul_f32_e32 v0, 0x42000000, v162
	s_waitcnt lgkmcnt(2)
	v_mul_f32_e32 v149, 0x42000000, v164
	v_med3_f32 v0, v0, s41, v143
	v_med3_f32 v149, v149, s41, v143
	v_mov_b32_e32 v151, 0
	v_cvt_pk_fp8_f32 v151, v0, v149
	ds_read2_b32 v[170:171], v148 offset0:40 offset1:56
	ds_read2_b32 v[172:173], v148 offset0:105 offset1:121
	ds_read2_b32 v[174:175], v148 offset0:170 offset1:186
	ds_read2_b32 v[176:177], v148 offset0:235 offset1:251
	s_waitcnt lgkmcnt(5)
	v_mul_f32_e32 v152, 0x42000000, v166
	s_waitcnt lgkmcnt(4)
	v_mul_f32_e32 v153, 0x42000000, v168
	v_med3_f32 v0, v152, s41, v143
	v_med3_f32 v149, v153, s41, v143
	v_cvt_pk_fp8_f32 v151, v0, v149 op_sel:[0,0,1]
	s_waitcnt lgkmcnt(3)
	v_mul_f32_e32 v0, 0x42000000, v170
	s_waitcnt lgkmcnt(2)
	v_mul_f32_e32 v149, 0x42000000, v172
	v_med3_f32 v0, v0, s41, v143
	v_med3_f32 v149, v149, s41, v143
	v_mov_b32_e32 v152, 0
	v_cvt_pk_fp8_f32 v152, v0, v149
	ds_read2_b32 v[178:179], v146 offset0:44 offset1:60
	ds_read2_b32 v[180:181], v146 offset0:109 offset1:125
	ds_read2_b32 v[182:183], v146 offset0:174 offset1:190
	s_waitcnt lgkmcnt(4)
	v_mul_f32_e32 v153, 0x42000000, v174
	s_waitcnt lgkmcnt(3)
	v_mul_f32_e32 v154, 0x42000000, v176
	v_med3_f32 v0, v153, s41, v143
	v_med3_f32 v149, v154, s41, v143
	ds_read2_b32 v[184:185], v146 offset0:239 offset1:255
	v_cvt_pk_fp8_f32 v152, v0, v149 op_sel:[0,0,1]
	s_waitcnt lgkmcnt(3)
	v_mul_f32_e32 v0, 0x42000000, v178
	s_waitcnt lgkmcnt(2)
	v_mul_f32_e32 v149, 0x42000000, v180
	v_med3_f32 v0, v0, s41, v143
	v_med3_f32 v149, v149, s41, v143
	v_mov_b32_e32 v153, 0
	v_cvt_pk_fp8_f32 v153, v0, v149
	s_waitcnt lgkmcnt(1)
	v_mul_f32_e32 v154, 0x42000000, v182
	s_waitcnt lgkmcnt(0)
	v_mul_f32_e32 v0, 0x42000000, v184
	v_med3_f32 v149, v154, s41, v143
	v_med3_f32 v0, v0, s41, v143
	v_cvt_pk_fp8_f32 v153, v149, v0 op_sel:[0,0,1]
	v_mul_f32_e32 v0, 0x42000000, v155
	v_mul_f32_e32 v149, 0x42000000, v157
	v_med3_f32 v0, v0, s41, v143
	v_med3_f32 v149, v149, s41, v143
	v_mov_b32_e32 v154, 0
	v_cvt_pk_fp8_f32 v154, v0, v149
	v_mul_f32_e32 v155, 0x42000000, v159
	v_mul_f32_e32 v0, 0x42000000, v161
	v_med3_f32 v149, v155, s41, v143
	v_med3_f32 v0, v0, s41, v143
	v_cvt_pk_fp8_f32 v154, v149, v0 op_sel:[0,0,1]
	v_mul_f32_e32 v0, 0x42000000, v163
	v_mul_f32_e32 v149, 0x42000000, v165
	v_med3_f32 v0, v0, s41, v143
	v_med3_f32 v149, v149, s41, v143
	v_mov_b32_e32 v155, 0
	v_cvt_pk_fp8_f32 v155, v0, v149
	v_mul_f32_e32 v156, 0x42000000, v167
	v_mul_f32_e32 v0, 0x42000000, v169
	v_med3_f32 v149, v156, s41, v143
	v_med3_f32 v0, v0, s41, v143
	v_cvt_pk_fp8_f32 v155, v149, v0 op_sel:[0,0,1]
	v_mul_f32_e32 v0, 0x42000000, v171
	v_mul_f32_e32 v149, 0x42000000, v173
	v_med3_f32 v0, v0, s41, v143
	v_med3_f32 v149, v149, s41, v143
	v_mov_b32_e32 v156, 0
	v_cvt_pk_fp8_f32 v156, v0, v149
	v_mul_f32_e32 v157, 0x42000000, v175
	v_mul_f32_e32 v0, 0x42000000, v177
	v_med3_f32 v149, v157, s41, v143
	v_med3_f32 v0, v0, s41, v143
	v_cvt_pk_fp8_f32 v156, v149, v0 op_sel:[0,0,1]
	v_mul_f32_e32 v0, 0x42000000, v179
	v_mul_f32_e32 v149, 0x42000000, v181
	v_med3_f32 v0, v0, s41, v143
	v_med3_f32 v149, v149, s41, v143
	v_mov_b32_e32 v157, 0
	v_cvt_pk_fp8_f32 v157, v0, v149
	v_mul_f32_e32 v158, 0x42000000, v183
	v_mul_f32_e32 v0, 0x42000000, v185
	v_med3_f32 v149, v158, s41, v143
	v_med3_f32 v0, v0, s41, v143
	v_cvt_pk_fp8_f32 v157, v149, v0 op_sel:[0,0,1]
	v_lshl_add_u64 v[2:3], v[2:3], 0, s[22:23]
	global_store_dwordx4 v[2:3], v[150:153], off
	v_lshl_add_u64 v[2:3], v[2:3], 0, s[22:23]
	global_store_dwordx4 v[2:3], v[154:157], off
	s_waitcnt lgkmcnt(0)
	s_cbranch_vccnz .LBB0_71
	s_add_i32 s42, s44, s48
	s_cmp_lt_i32 s42, 0x1ac0
	s_cbranch_scc1 .Lpt_2
	s_cmp_ge_i32 s42, 0xe580
	s_cbranch_scc1 .Lpt_2
	s_add_i32 s42, s42, 0xcac0

;     ...
;         auto decode = [&](int it) -> TrDesc {
;             TrDesc d; d.zero = 0; d.rope = 0; d.f8 = 0;
;             const int l = it / C_L; int r = it % C_L;
;             const float* W; unsigned char* WT; int ldw, K, k0, n0, scol, esz = 2;
;             if (r < C_IN) { const int kb = r / 188, nb = r % 188; n0 = 64 * nb; k0 = 64 * kb; ldw = NIN; K = D; W = a.w_in + (size_t)l * D * NIN;
;                 if (n0 < 3072) { d.rope = 1; scol = (n0 >> 7) * 128 + 32 * ((n0 >> 6) & 1) + 64 * (q4 >> 3) + 4 * (q4 & 7); }
;                 else if (n0 < 7680) scol = n0 + 4 * q4;
;                 else if (n0 < 11776) scol = n0 + 16 + 4 * q4;
;                 else if (n0 == 11776) { scol = (q4 < 4) ? 7680 + 4 * q4 : 0; d.zero = (q4 < 4) ? 0 : 1; }
;                 else { scol = 0; d.zero = 1; }
;     ...
;                 d.f8 = 1; esz = 1; WT = ws + WS_WIN + (size_t)l * NP * D;
;     ...
;                 WT = ws + WS_WIN + (size_t)l * NP * D * 2;
;     ...
;             } else if ((r -= C_IN) < C_OA) { const int kb = r / 32, nb = r % 32; n0 = 64 * nb; k0 = 64 * kb; ldw = D; K = 512; scol = n0 + 4 * q4; W = a.w_out_a + (size_t)l * 512 * D; WT = ws + WS_WOA + (size_t)l * D * 512 * (MIX_F8 ? 1 : 2); if (MIX_F8) { d.f8 = 1; esz = 1; }
;                 if (BR_FUSE) { K = 1536; WT = ws + WS_WOA + (size_t)l * D * 1536 + 1024; }
;             } else if ((r -= C_OA) < C_OB) { const int kb = r / 32, nb = r % 32; n0 = 64 * nb; k0 = 64 * kb; ldw = D; K = 1024; scol = n0 + 4 * q4; W = a.w_out_b + (size_t)l * 1024 * D; WT = ws + WS_WOB + (size_t)l * D * 1024 * (MIX_F8 ? 1 : 2); if (MIX_F8) { d.f8 = 1; esz = 1; }
;                 if (BR_FUSE) { K = 1536; WT = ws + WS_WOA + (size_t)l * D * 1536; }
; template <unsigned MASK, bool ONE>
; __global__ void __launch_bounds__(NTHREADS, 2) fwd_kernel(Args a_unused) {
;     ...
;         if (IN(P + 1, 2)) { FRESH_TID();
;     ...
;             pg8::StaticOrderP S{T / 256, NP / 256, G, bx}; pg8::RowsContig AM; pg8::EpiProj E{proj, ropec, ropes, alow, pg8::W8_INV};
;             pg8::gemm_phase<pg8::EpiProj, pg8::StaticOrderP, pg8::RowsContig, true, true>(lds, tid, hbuf, (const bf16_t*)(ws + WS_WIN + (size_t)l * NP * D), 0, D / 2, S, AM, E);
.LBB0_265:
	s_or_b64 exec, exec, s[0:1]
	v_readlane_b32 s0, v253, 0
	v_readlane_b32 s1, v253, 1
	s_mov_b32 s2, s38
	s_waitcnt lgkmcnt(0)
	s_barrier
	s_nop 0
	v_mbcnt_lo_u32_b32 v0, s2, 0
	v_mbcnt_hi_u32_b32 v0, s2, v0
	v_readlane_b32 s2, v253, 7
	v_readlane_b32 s3, v253, 8
	v_add_u32_e32 v1, s78, v0
	s_andn2_b64 vcc, exec, s[2:3]
	v_readfirstlane_b32 s16, v1
	v_readlane_b32 s101, v255, 17
	s_movk_i32 s100, 0x100
	s_cmp_eq_u32 s101, 0
	s_cbranch_scc0 .Lpq_skip
	s_movk_i32 s100, 0xd8
	v_readlane_b32 s101, v253, 4
	s_nop 1
	s_cmp_lt_i32 s101, s100
	s_cbranch_scc1 .Lpq_skip
	s_mov_b32 s100, 0x9e80
	s_mov_b32 s101, 0xe580
	v_writelane_b32 v251, s16, 0
	v_writelane_b32 v251, s17, 1
	v_writelane_b32 v251, s18, 2
	v_writelane_b32 v251, s19, 3
	v_writelane_b32 v251, s20, 4
	v_writelane_b32 v251, s21, 5
	v_writelane_b32 v251, s23, 6
	v_writelane_b32 v251, s25, 7
	v_writelane_b32 v251, s26, 8
	v_writelane_b32 v251, s33, 9
	v_writelane_b32 v251, s38, 10
	v_writelane_b32 v251, s39, 11
	v_writelane_b32 v251, s41, 12
	v_writelane_b32 v251, s42, 13
	v_writelane_b32 v251, s45, 14
	v_writelane_b32 v251, s48, 15
	v_writelane_b32 v251, s49, 16
	v_writelane_b32 v251, s50, 17
	v_writelane_b32 v251, s51, 18
	v_writelane_b32 v251, s74, 19
	v_writelane_b32 v251, s76, 20
	v_mov_b32_e32 v193, v3
	v_mov_b32_e32 v194, v33
	v_mov_b32_e32 v195, v59
	v_mov_b32_e32 v196, v63
	v_mov_b32_e32 v197, v110
	v_mov_b32_e32 v198, v111
	v_mov_b32_e32 v199, v114
	v_mov_b32_e32 v200, v115
	v_mov_b32_e32 v201, v149
	v_mov_b32_e32 v202, v153
	v_mov_b32_e32 v203, v157
	v_mov_b32_e32 v204, v161
	v_mov_b32_e32 v205, v165
	v_mov_b32_e32 v206, v169
	v_mov_b32_e32 v207, v173
	v_mov_b32_e32 v208, v177
	v_mov_b32_e32 v209, v178
	v_mov_b32_e32 v210, v179
	v_mov_b32_e32 v211, v180
	v_mov_b32_e32 v212, v181
	v_mov_b32_e32 v214, v182
	v_mov_b32_e32 v215, v183
	v_mov_b32_e32 v216, v184
	v_mov_b32_e32 v218, v185
	v_readlane_b32 s76, v253, 4
	v_readlane_b32 s8, v253, 0
	v_readlane_b32 s9, v253, 1
	s_nop 1
	s_sub_i32 s0, s76, 216
	s_lshr_b32 s1, s100, 3
	s_add_i32 s0, s0, s1
	s_lshr_b32 s33, s78, 6
	s_lshr_b32 s1, s0, 3
	s_lshl_b32 s1, s1, 6
	s_and_b32 s0, s0, 7
	s_lshl_b32 s0, s0, 2
	s_or_b32 s1, s1, s0
	s_and_b32 s0, s33, 3
	s_or_b32 s1, s1, s0
	s_lshr_b32 s0, s33, 2
	s_lshl_b32 s0, s0, 5
	s_or_b32 s1, s1, s0
	s_sub_i32 s100, s1, s33
	s_mov_b32 s76, 0
	s_movk_i32 s74, 40
	s_load_dwordx2 s[10:11], s[8:9], 0xa0
	v_mbcnt_lo_u32_b32 v69, -1, 0
	v_mbcnt_hi_u32_b32 v69, -1, v69
	s_mov_b64 exec, -1
	v_lshlrev_b32_e32 v76, 3, v69
	s_waitcnt lgkmcnt(0)
	s_lshl_b32 s47, s76, 3
	s_add_i32 s47, s47, s33
	s_add_i32 s47, s47, s100
	v_and_b32_e32 v2, 15, v69
	s_cmp_ge_i32 s47, s101
	v_ashrrev_i32_e32 v133, 4, v69
	s_cbranch_scc1 .LBB0_36_hq
	s_sub_i32 s1, 0xfcff, s47
	s_mul_hi_u32 s0, s1, 0x81848da9
	s_lshr_b32 s0, s0, 14
	s_mul_i32 s2, s0, 0x7e80
	s_sub_i32 s17, s1, s2
	s_cmpk_gt_u32 s17, 0x177f
	s_cbranch_scc0 .LBB0_37_hq
	s_cmpk_gt_u32 s17, 0x187f
	s_cbranch_scc0 .LBB0_39_hq
	s_cmpk_gt_u32 s17, 0x1a7f
	s_cbranch_scc0 .LBB0_40_hq
	s_cmpk_gt_u32 s17, 0x1e7f
	s_cbranch_scc0 .LBB0_41_hq
	s_lshl_b32 s1, s17, 6
	s_cmpk_gt_u32 s17, 0x5e7f
	s_cbranch_scc0 .LBB0_42_hq
	s_add_i32 s2, s17, 0xffffa180
	s_lshr_b32 s4, s2, 9
	s_lshl_b32 s2, s2, 1
	s_and_b32 s18, s2, 0x3c0
	s_load_dwordx2 s[2:3], s[8:9], 0x88
	s_lshl_b32 s5, s0, 4
	s_add_i32 s6, s4, s5
	s_mov_b32 s7, 0
	s_and_b32 s16, s1, 0x7c0
	s_lshl_b64 s[4:5], s[6:7], 23
	s_waitcnt lgkmcnt(0)
	s_add_u32 s4, s2, s4
	s_addc_u32 s5, s3, s5
	s_lshl_b64 s[2:3], s[6:7], 21
	s_add_u32 s2, s10, s2
	s_addc_u32 s3, s11, s3
	s_add_u32 s6, s2, 0x18600000
	v_lshl_or_b32 v0, v2, 2, s16
	s_addc_u32 s7, s3, 0
	s_mov_b64 s[2:3], 0
	s_branch .LBB0_43_hq

; #define LAS __attribute__((address_space(3)))
; #define FRESH_TID() do { ap = fresh_args(); ws = ap->ws; unsigned m1_ = ~0u; asm volatile("" : "+s"(m1_)); lane = (int)__builtin_amdgcn_mbcnt_hi(m1_, __builtin_amdgcn_mbcnt_lo(m1_, 0u)); asm volatile("" : "+v"(lane)); wave = wave0; tid = wave0 * 64 + lane; } while (0)
; __device__ __forceinline__ void moe_table_build(LAS unsigned char* lds, const unsigned* cnt, int tid) {
;     if (tid < NE) { const int n = (int)__hip_atomic_load(cnt + 64 * tid, RLX_AGENT); ((LAS int*)(lds + MOE_TAB_OFF))[16 + tid] = n; }
; template <unsigned MASK, bool ONE>
; __global__ void __launch_bounds__(NTHREADS, 2) fwd_kernel(Args a_unused) {
;     ...
;         if (IN(P + 8, 9)) { FRESH_TID();
;             pg8::moe_table_build(lds, cntl, tid);
.LBB0_925:
	s_or_b64 exec, exec, s[0:1]
	v_readlane_b32 s101, v255, 17
	s_movk_i32 s100, 0x100
	s_cmp_eq_u32 s101, 0
	s_cselect_b32 s100, 0xa0, s100
	s_cselect_b32 s101, 96, 0
	v_readlane_b32 s0, v253, 0
	v_readlane_b32 s1, v253, 1
	s_waitcnt lgkmcnt(0)
	s_barrier
	s_load_dwordx2 s[6:7], s[0:1], 0xa0
	s_mov_b32 s0, s38
	s_nop 0
	v_mbcnt_lo_u32_b32 v0, s0, 0
	v_mbcnt_hi_u32_b32 v0, s0, v0
	s_nop 0
	v_add_u32_e32 v1, s78, v0
	v_cmp_gt_i32_e32 vcc, 16, v1
	s_and_saveexec_b64 s[0:1], vcc
	s_cbranch_execz .LBB0_927
	s_lshl_b64 s[2:3], s[96:97], 2
	s_waitcnt lgkmcnt(0)
	s_add_u32 s2, s6, s2
	v_lshlrev_b32_e32 v2, 6, v1
	s_addc_u32 s3, s7, s3
	v_ashrrev_i32_e32 v3, 31, v2
	v_lshl_add_u64 v[2:3], v[2:3], 2, s[2:3]
	v_add_co_u32_e32 v2, vcc, 0x10000, v2
	v_readlane_b32 s2, v255, 23
	s_nop 0
	v_addc_co_u32_e32 v3, vcc, 0, v3, vcc
	global_load_dword v2, v[2:3], off sc1
	v_lshl_add_u32 v3, v1, 2, s2
	s_waitcnt vmcnt(0)
	ds_write_b32 v3, v2 offset:64

; #define LAS __attribute__((address_space(3)))
; __device__ __forceinline__ void moe_table_build(LAS unsigned char* lds, const unsigned* cnt, int tid) {
;     ...
;     __syncthreads();
;     if (tid == 0) { int acc = 0; for (int e = 0; e < NE; ++e) { acc += (((LAS int*)(lds + MOE_TAB_OFF))[16 + e] + 255) >> 8; ((LAS int*)(lds + MOE_TAB_OFF))[e] = acc; } }
;     __syncthreads();
; }
;     __device__ __forceinline__ void init(LAS unsigned char* lds_, int nN_, int G_, int c_) {
;         lds = lds_; NT = __builtin_amdgcn_readfirstlane(((LAS int*)(lds + MOE_TAB_OFF))[15]); nN = nN_; G = G_; c = c_; }
.LBB0_929:
	s_or_b64 exec, exec, s[0:1]
	v_readlane_b32 s0, v254, 58
	s_waitcnt lgkmcnt(0)
	s_barrier
	v_mov_b32_e32 v2, s0
	ds_read_b32 v2, v2
	v_readlane_b32 s1, v253, 4
	v_readfirstlane_b32 s14, v1
	s_waitcnt lgkmcnt(0)
	v_readfirstlane_b32 s22, v2
	s_lshl_b32 s0, s22, 3
	s_cmp_eq_u32 s101, 0
	s_cbranch_scc1 .Lno_help9
	s_cmpk_lt_i32 s1, 0xa0
	s_cbranch_scc1 .Lno_help9
	s_mov_b32 s100, 0x3cc0
	s_mov_b32 s101, 0x9e80
	s_mov_b32 s0, 0
	v_writelane_b32 v251, s0, 30
	s_movk_i32 s0, 96
	s_branch .Lhp_entry

; #define LAS __attribute__((address_space(3)))
;     ...
;         LAS float* scr = (LAS float*)(lds + wave * 16640);
;         const int gw = vcu * NWAVES + wave, NGW = G * NWAVES;
;         constexpr int C_IN = 32 * 188, C_OA = 8 * 32, C_OB = 16 * 32, C_O = 32 * 32, C_GU = 16 * 32 * 32, C_DN = 16 * 16 * 32, C_L = C_IN + C_OA + C_OB + C_O + C_GU + C_DN, NIT = DEPTH * C_L;
;         const int q4 = lane & 15, kk = lane >> 4;
;     ...
;         int it = gw; TrDesc dA, dB; f32x4 vA[16], vB[16];
;         if (it < NIT) { dA = decode(NIT - 1 - it); tr_load(dA, vA); }
.Lhp_entry:
	v_writelane_b32 v251, s16, 0
	v_writelane_b32 v251, s17, 1
	v_writelane_b32 v251, s18, 2
	v_writelane_b32 v251, s19, 3
	v_writelane_b32 v251, s20, 4
	v_writelane_b32 v251, s21, 5
	v_writelane_b32 v251, s23, 6
	v_writelane_b32 v251, s25, 7
	v_writelane_b32 v251, s26, 8
	v_writelane_b32 v251, s33, 9
	v_writelane_b32 v251, s38, 10
	v_writelane_b32 v251, s39, 11
	v_writelane_b32 v251, s41, 12
	v_writelane_b32 v251, s42, 13
	v_writelane_b32 v251, s45, 14
	v_writelane_b32 v251, s48, 15
	v_writelane_b32 v251, s49, 16
	v_writelane_b32 v251, s50, 17
	v_writelane_b32 v251, s51, 18
	v_writelane_b32 v251, s74, 19
	v_writelane_b32 v251, s76, 20
	v_mov_b32_e32 v193, v3
	v_mov_b32_e32 v194, v33
	v_mov_b32_e32 v195, v59
	v_mov_b32_e32 v196, v63
	v_mov_b32_e32 v197, v110
	v_mov_b32_e32 v198, v111
	v_mov_b32_e32 v199, v114
	v_mov_b32_e32 v200, v115
	v_mov_b32_e32 v201, v149
	v_mov_b32_e32 v202, v153
	v_mov_b32_e32 v203, v157
	v_mov_b32_e32 v204, v161
	v_mov_b32_e32 v205, v165
	v_mov_b32_e32 v206, v169
	v_mov_b32_e32 v207, v173
	v_mov_b32_e32 v208, v177
	v_mov_b32_e32 v209, v178
	v_mov_b32_e32 v210, v179
	v_mov_b32_e32 v211, v180
	v_mov_b32_e32 v212, v181
	v_mov_b32_e32 v214, v182
	v_mov_b32_e32 v215, v183
	v_mov_b32_e32 v216, v184
	v_mov_b32_e32 v218, v185
	s_mov_b32 s74, s0
	v_readlane_b32 s76, v253, 4
	v_readlane_b32 s8, v253, 0
	v_readlane_b32 s9, v253, 1
	s_nop 1
	s_add_i32 s0, s76, s74
	s_sub_i32 s0, s0, 0x100
	s_lshr_b32 s1, s100, 4
	s_add_i32 s0, s0, s1
	s_lshr_b32 s33, s78, 6
	s_lshr_b32 s1, s0, 2
	s_lshl_b32 s1, s1, 6
	s_and_b32 s0, s0, 3
	s_lshl_b32 s0, s0, 3
	s_or_b32 s100, s1, s0
	s_mov_b32 s76, 0
	s_load_dwordx2 s[10:11], s[8:9], 0xa0
	v_mbcnt_lo_u32_b32 v69, -1, 0
	v_mbcnt_hi_u32_b32 v69, -1, v69
	s_mov_b64 exec, -1
	v_lshlrev_b32_e32 v76, 3, v69
	s_waitcnt lgkmcnt(0)
	s_lshl_b32 s47, s76, 3
	s_add_i32 s47, s47, s33
	s_add_i32 s47, s47, s100
	v_and_b32_e32 v2, 15, v69
	s_cmp_ge_i32 s47, s101
	v_ashrrev_i32_e32 v133, 4, v69
	s_cbranch_scc1 .LBB0_36_hp
	s_sub_i32 s1, 0xfcff, s47
	s_mul_hi_u32 s0, s1, 0x81848da9
	s_lshr_b32 s0, s0, 14
	s_mul_i32 s2, s0, 0x7e80
	s_sub_i32 s17, s1, s2
	s_cmpk_gt_u32 s17, 0x177f
	s_cbranch_scc0 .LBB0_37_hp
	s_cmpk_gt_u32 s17, 0x187f
	s_cbranch_scc0 .LBB0_39_hp
	s_cmpk_gt_u32 s17, 0x1a7f
	s_cbranch_scc0 .LBB0_40_hp
	s_cmpk_gt_u32 s17, 0x1e7f
	s_cbranch_scc0 .LBB0_41_hp
	s_lshl_b32 s1, s17, 6
	s_cmpk_gt_u32 s17, 0x5e7f
	s_cbranch_scc0 .LBB0_42_hp
	s_add_i32 s2, s17, 0xffffa180
	s_lshr_b32 s4, s2, 9
	s_lshl_b32 s2, s2, 1
	s_and_b32 s18, s2, 0x3c0
	s_load_dwordx2 s[2:3], s[8:9], 0x88
	s_lshl_b32 s5, s0, 4
	s_add_i32 s6, s4, s5
	s_mov_b32 s7, 0
	s_and_b32 s16, s1, 0x7c0
	s_lshl_b64 s[4:5], s[6:7], 23
	s_waitcnt lgkmcnt(0)
	s_add_u32 s4, s2, s4
	s_addc_u32 s5, s3, s5
	s_lshl_b64 s[2:3], s[6:7], 21
	s_add_u32 s2, s10, s2
	s_addc_u32 s3, s11, s3
	s_add_u32 s6, s2, 0x18600000
	v_lshl_or_b32 v0, v2, 2, s16
	s_addc_u32 s7, s3, 0
	s_mov_b64 s[2:3], 0
	s_branch .LBB0_43_hp

;     ...
;         auto decode = [&](int it) -> TrDesc {
;             TrDesc d; d.zero = 0; d.rope = 0; d.f8 = 0;
;             const int l = it / C_L; int r = it % C_L;
;             const float* W; unsigned char* WT; int ldw, K, k0, n0, scol, esz = 2;
;             if (r < C_IN) { const int kb = r / 188, nb = r % 188; n0 = 64 * nb; k0 = 64 * kb; ldw = NIN; K = D; W = a.w_in + (size_t)l * D * NIN;
;                 if (n0 < 3072) { d.rope = 1; scol = (n0 >> 7) * 128 + 32 * ((n0 >> 6) & 1) + 64 * (q4 >> 3) + 4 * (q4 & 7); }
;                 else if (n0 < 7680) scol = n0 + 4 * q4;
;                 else if (n0 < 11776) scol = n0 + 16 + 4 * q4;
;                 else if (n0 == 11776) { scol = (q4 < 4) ? 7680 + 4 * q4 : 0; d.zero = (q4 < 4) ? 0 : 1; }
;                 else { scol = 0; d.zero = 1; }
;     ...
;                 d.f8 = 1; esz = 1; WT = ws + WS_WIN + (size_t)l * NP * D;
;     ...
;                 WT = ws + WS_WIN + (size_t)l * NP * D * 2;
;     ...
;             } else if ((r -= C_IN) < C_OA) { const int kb = r / 32, nb = r % 32; n0 = 64 * nb; k0 = 64 * kb; ldw = D; K = 512; scol = n0 + 4 * q4; W = a.w_out_a + (size_t)l * 512 * D; WT = ws + WS_WOA + (size_t)l * D * 512 * (MIX_F8 ? 1 : 2); if (MIX_F8) { d.f8 = 1; esz = 1; }
;                 if (BR_FUSE) { K = 1536; WT = ws + WS_WOA + (size_t)l * D * 1536 + 1024; }
;             } else if ((r -= C_OA) < C_OB) { const int kb = r / 32, nb = r % 32; n0 = 64 * nb; k0 = 64 * kb; ldw = D; K = 1024; scol = n0 + 4 * q4; W = a.w_out_b + (size_t)l * 1024 * D; WT = ws + WS_WOB + (size_t)l * D * 1024 * (MIX_F8 ? 1 : 2); if (MIX_F8) { d.f8 = 1; esz = 1; }
;                 if (BR_FUSE) { K = 1536; WT = ws + WS_WOA + (size_t)l * D * 1536; }
;             } else if ((r -= C_OB) < C_O) { const int kb = r / 32, nb = r % 32; n0 = 64 * nb; k0 = 64 * kb; ldw = D; K = D; scol = n0 + 4 * q4; W = a.w_out + (size_t)l * D * D; WT = ws + WS_WO + (size_t)l * D * D * (MIX_F8 ? 1 : 2); if (MIX_F8) { d.f8 = 1; esz = 1; }
;             } else if ((r -= C_O) < C_GU) { const int e = r / 1024, r2 = r % 1024, kb = r2 / 32, nb = r2 % 32, pn = nb >> 2, sgu = (nb >> 1) & 1, c0 = 64 * (nb & 1);
;                 n0 = 64 * nb; k0 = 64 * kb; ldw = FF; K = D; scol = 128 * pn + c0 + 4 * q4; W = (sgu ? a.w_up_e : a.w_gate_e) + (size_t)(l * NE + e) * D * FF; WT = ws + WS_WGU + (size_t)(l * NE + e) * 2048 * D; d.f8 = 1; esz = 1;
.LBB0_72_hp:
	s_cmp_ge_i32 s42, s101
	s_cbranch_scc1 .LBB0_70_hp
	s_bitcmp1_b32 s42, 5
	s_cbranch_scc1 .Ladv44_else_hp
	s_add_i32 s44, s42, 32
	s_branch .Ladv44_end_hp
.Ladv44_else_hp:
	s_lshr_b32 s44, s42, 6
	s_lshl_b32 s44, s44, 2
	s_bfe_u32 s100, s42, 0x20003
	s_or_b32 s44, s44, s100
	s_add_i32 s44, s44, s74
	s_and_b32 s100, s44, 3
	s_lshr_b32 s44, s44, 2
	s_lshl_b32 s44, s44, 6
	s_lshl_b32 s100, s100, 3
	s_or_b32 s44, s44, s100
	s_and_b32 s100, s42, 7
	s_or_b32 s44, s44, s100
.Ladv44_end_hp:
	s_cmp_lt_i32 s44, s101
	s_cselect_b64 s[20:21], -1, 0
	s_cmp_ge_i32 s44, s101
	s_cselect_b64 s[12:13], -1, 0
	s_and_b64 vcc, exec, s[12:13]
	s_cbranch_vccnz .LBB0_106_hp
	s_sub_i32 s3, 0xfcff, s44
	s_mul_hi_u32 s0, s3, 0x81848da9
	s_lshr_b32 s0, s0, 14
	s_mul_i32 s14, s0, 0x7e80
	s_sub_i32 s45, s3, s14
	s_cmpk_gt_u32 s45, 0x177f
	s_cbranch_scc0 .LBB0_81_hp
	s_cmpk_gt_u32 s45, 0x187f
	s_cbranch_scc0 .LBB0_83_hp
	s_cmpk_gt_u32 s45, 0x1a7f
	s_cbranch_scc0 .LBB0_84_hp
	s_cmpk_gt_u32 s45, 0x1e7f
	s_cbranch_scc0 .LBB0_85_hp
	s_lshl_b32 s24, s45, 6
	s_cmpk_gt_u32 s45, 0x5e7f
	s_cbranch_scc0 .LBB0_121_hp
	s_add_i32 s14, s45, 0xffffa180
	s_lshr_b32 s18, s14, 9
	s_lshl_b32 s14, s14, 1
	s_and_b32 s49, s14, 0x3c0
	s_load_dwordx2 s[14:15], s[8:9], 0x88
	s_lshl_b32 s19, s0, 4
	s_add_i32 s22, s18, s19
	s_mov_b32 s23, s1
	s_and_b32 s3, s24, 0x7c0
	s_lshl_b64 s[18:19], s[22:23], 23
	s_waitcnt lgkmcnt(0)
	s_add_u32 s18, s14, s18
	s_addc_u32 s19, s15, s19
	s_lshl_b64 s[14:15], s[22:23], 21
	s_add_u32 s22, s28, s14
	v_or_b32_e32 v0, s3, v136
	s_addc_u32 s23, s29, s15
	s_cbranch_execz .LBB0_122_hp
	s_movk_i32 s14, 0x400
	s_mov_b64 s[24:25], 0x800
	s_cbranch_execz .LBB0_86_hp
	s_branch .LBB0_87_hp

; #define LAS __attribute__((address_space(3)))
; #define GAS __attribute__((address_space(1)))
; #define LDS_WAIT() asm volatile("s_waitcnt lgkmcnt(0)" ::: "memory")
; __device__ __forceinline__ unsigned pk_fp8x4(float a, float b, float c, float d) { int p = __builtin_amdgcn_cvt_pk_fp8_f32(sat8(a), sat8(b), 0, false); p = __builtin_amdgcn_cvt_pk_fp8_f32(sat8(c), sat8(d), p, true); return (unsigned)p; }
; __device__ __forceinline__ void tr_finish(const TrDesc& d, f32x4 (&v)[16], LAS float* scr, int lane) {
;     const int kk = lane >> 4, q4 = lane & 15;
;     if (d.zero) {
; #pragma unroll
;         for (int i = 0; i < 16; ++i) v[i] = (f32x4){0.f, 0.f, 0.f, 0.f}; }
;     const int d0 = d.rope ? 8 * (q4 & 7) + (q4 >> 3) : 4 * q4, ds = d.rope ? 2 : 1;
;     { LAS float* rp = scr + kk * 65 + d0;
; #pragma unroll
;         for (int i = 0; i < 16; ++i) { rp[4 * i * 65] = v[i][0]; rp[4 * i * 65 + ds] = v[i][1]; rp[4 * i * 65 + 2 * ds] = v[i][2]; rp[4 * i * 65 + 3 * ds] = v[i][3]; } }
;     LDS_WAIT(); asm volatile("" ::: "memory");
;     if (d.f8) {
;         const int c = lane & 3, nl = lane >> 2; const LAS float* sp = scr + (16 * c) * 65 + nl; unsigned char* dp = d.dst + (size_t)nl * d.K + 16 * c;
; #pragma unroll
;         for (int j = 0; j < 4; ++j) { u32x4 o;
;             o.x = pk_fp8x4(sp[0 * 65 + 16 * j] * 32.0f, sp[1 * 65 + 16 * j] * 32.0f, sp[2 * 65 + 16 * j] * 32.0f, sp[3 * 65 + 16 * j] * 32.0f);
;             o.y = pk_fp8x4(sp[4 * 65 + 16 * j] * 32.0f, sp[5 * 65 + 16 * j] * 32.0f, sp[6 * 65 + 16 * j] * 32.0f, sp[7 * 65 + 16 * j] * 32.0f);
;             o.z = pk_fp8x4(sp[8 * 65 + 16 * j] * 32.0f, sp[9 * 65 + 16 * j] * 32.0f, sp[10 * 65 + 16 * j] * 32.0f, sp[11 * 65 + 16 * j] * 32.0f);
;             o.w = pk_fp8x4(sp[12 * 65 + 16 * j] * 32.0f, sp[13 * 65 + 16 * j] * 32.0f, sp[14 * 65 + 16 * j] * 32.0f, sp[15 * 65 + 16 * j] * 32.0f);
;             *(GAS u32x4*)(dp + (size_t)(16 * j) * d.K) = o; }
.LBB0_108_hp:
	s_or_b64 exec, exec, s[22:23]
	s_cmp_eq_u32 s43, 0
	s_cselect_b64 vcc, -1, 0
	s_cmp_lg_u32 s43, 0
	s_cselect_b64 s[22:23], -1, 0
	v_cndmask_b32_e64 v2, 0, 1, s[22:23]
	s_and_b64 s[22:23], s[22:23], exec
	v_cndmask_b32_e32 v0, v140, v136, vcc
	s_cselect_b32 s0, 2, 1
	v_lshl_add_u32 v0, v0, 2, v141
	s_lshl_b32 s3, s0, 2
	v_add_u32_e32 v3, s3, v0
	v_lshlrev_b32_e64 v2, v2, 3
	s_waitcnt vmcnt(15)
	ds_write_b32 v3, v5
	v_lshl_add_u32 v3, s0, 3, v0
	v_lshl_add_u32 v2, v2, 2, v0
	v_subrev_u32_e32 v146, s3, v3
	ds_write_b32 v0, v4
	ds_write_b32 v3, v6
	ds_write_b32 v2, v7
	s_waitcnt vmcnt(14)
	ds_write_b32 v0, v8 offset:1040
	ds_write_b32 v146, v9 offset:1040
	ds_write_b32 v3, v10 offset:1040
	ds_write_b32 v2, v11 offset:1040
	s_waitcnt vmcnt(13)
	ds_write_b32 v0, v12 offset:2080
	ds_write_b32 v146, v13 offset:2080
	ds_write_b32 v3, v14 offset:2080
	ds_write_b32 v2, v15 offset:2080
	s_waitcnt vmcnt(12)
	ds_write_b32 v0, v16 offset:3120
	ds_write_b32 v146, v17 offset:3120
	ds_write_b32 v3, v18 offset:3120
	ds_write_b32 v2, v19 offset:3120
	s_waitcnt vmcnt(11)
	ds_write_b32 v0, v20 offset:4160
	ds_write_b32 v146, v21 offset:4160
	ds_write_b32 v3, v22 offset:4160
	ds_write_b32 v2, v23 offset:4160
	s_waitcnt vmcnt(10)
	ds_write_b32 v0, v24 offset:5200
	ds_write_b32 v146, v25 offset:5200
	ds_write_b32 v3, v26 offset:5200
	ds_write_b32 v2, v27 offset:5200
	s_waitcnt vmcnt(9)
	ds_write_b32 v0, v28 offset:6240
	ds_write_b32 v146, v29 offset:6240
	ds_write_b32 v3, v30 offset:6240
	ds_write_b32 v2, v31 offset:6240
	s_waitcnt vmcnt(8)
	ds_write_b32 v0, v32 offset:7280
	ds_write_b32 v146, v33 offset:7280
	ds_write_b32 v3, v34 offset:7280
	ds_write_b32 v2, v35 offset:7280
	s_waitcnt vmcnt(7)
	ds_write_b32 v0, v36 offset:8320
	ds_write_b32 v146, v37 offset:8320
	ds_write_b32 v3, v38 offset:8320
	ds_write_b32 v2, v39 offset:8320
	s_waitcnt vmcnt(6)
	ds_write_b32 v0, v40 offset:9360
	ds_write_b32 v146, v41 offset:9360
	ds_write_b32 v3, v42 offset:9360
	ds_write_b32 v2, v43 offset:9360
	s_waitcnt vmcnt(5)
	ds_write_b32 v0, v44 offset:10400
	ds_write_b32 v146, v45 offset:10400
	ds_write_b32 v3, v46 offset:10400
	ds_write_b32 v2, v47 offset:10400
	s_waitcnt vmcnt(4)
	ds_write_b32 v0, v48 offset:11440
	ds_write_b32 v146, v49 offset:11440
	ds_write_b32 v3, v50 offset:11440
	ds_write_b32 v2, v51 offset:11440
	s_waitcnt vmcnt(3)
	ds_write_b32 v0, v52 offset:12480
	ds_write_b32 v146, v53 offset:12480
	ds_write_b32 v3, v54 offset:12480
	ds_write_b32 v2, v55 offset:12480
	s_waitcnt vmcnt(2)
	ds_write_b32 v0, v56 offset:13520
	ds_write_b32 v146, v57 offset:13520
	ds_write_b32 v3, v58 offset:13520
	ds_write_b32 v2, v59 offset:13520
	s_waitcnt vmcnt(1)
	ds_write_b32 v0, v60 offset:14560
	ds_write_b32 v146, v61 offset:14560
	ds_write_b32 v3, v62 offset:14560
	ds_write_b32 v2, v63 offset:14560
	s_waitcnt vmcnt(0)
	ds_write_b32 v0, v64 offset:15600
	ds_write_b32 v146, v65 offset:15600
	ds_write_b32 v3, v66 offset:15600
	ds_write_b32 v2, v67 offset:15600
	s_waitcnt lgkmcnt(0)
	ds_read2_b32 v[2:3], v142 offset1:16
	ds_read2_b32 v[148:149], v142 offset0:65 offset1:81
	ds_read2_b32 v[154:155], v142 offset0:130 offset1:146
	ds_read2_b32 v[156:157], v142 offset0:195 offset1:211
	v_mov_b32_e32 v150, 0
	s_waitcnt lgkmcnt(3)
	v_mul_f32_e32 v0, 0x42000000, v2
	s_waitcnt lgkmcnt(2)
	v_mul_f32_e32 v2, 0x42000000, v148
	v_med3_f32 v0, v0, s41, v143
	s_waitcnt lgkmcnt(0)
	v_mul_f32_e32 v147, 0x42000000, v156
	v_med3_f32 v2, v2, s41, v143
	v_cvt_pk_fp8_f32 v150, v0, v2
	v_med3_f32 v2, v147, s41, v143
	v_add_u32_e32 v147, 0x400, v142
	ds_read2_b32 v[160:161], v147 offset0:4 offset1:20
	ds_read2_b32 v[162:163], v147 offset0:69 offset1:85
	ds_read2_b32 v[164:165], v147 offset0:134 offset1:150
	ds_read2_b32 v[166:167], v147 offset0:199 offset1:215
	v_mul_f32_e32 v146, 0x42000000, v154
	v_med3_f32 v0, v146, s41, v143
	v_cvt_pk_fp8_f32 v150, v0, v2 op_sel:[0,0,1]
	s_waitcnt lgkmcnt(3)
	v_mul_f32_e32 v0, 0x42000000, v160
	s_waitcnt lgkmcnt(2)
	v_mul_f32_e32 v2, 0x42000000, v162
	s_waitcnt lgkmcnt(0)
	v_mul_f32_e32 v148, 0x42000000, v166
	v_med3_f32 v0, v0, s41, v143
	v_med3_f32 v2, v2, s41, v143
	v_mov_b32_e32 v151, 0
	v_cvt_pk_fp8_f32 v151, v0, v2
	v_med3_f32 v2, v148, s41, v143
	v_add_u32_e32 v148, 0x800, v142
	ds_read2_b32 v[168:169], v148 offset0:8 offset1:24
	ds_read2_b32 v[170:171], v148 offset0:73 offset1:89
	ds_read2_b32 v[172:173], v148 offset0:138 offset1:154
	ds_read2_b32 v[174:175], v148 offset0:203 offset1:219
	v_mul_f32_e32 v146, 0x42000000, v164
	v_med3_f32 v0, v146, s41, v143
	v_cvt_pk_fp8_f32 v151, v0, v2 op_sel:[0,0,1]
	s_waitcnt lgkmcnt(3)
	v_mul_f32_e32 v0, 0x42000000, v168
	s_waitcnt lgkmcnt(2)
	v_mul_f32_e32 v2, 0x42000000, v170
	s_waitcnt lgkmcnt(1)
	v_mul_f32_e32 v146, 0x42000000, v172
	v_med3_f32 v0, v0, s41, v143
	v_med3_f32 v2, v2, s41, v143
	v_mov_b32_e32 v152, 0
	v_cvt_pk_fp8_f32 v152, v0, v2
	v_med3_f32 v0, v146, s41, v143
	v_add_u32_e32 v146, 0xc00, v142
	ds_read2_b32 v[176:177], v146 offset0:12 offset1:28
	ds_read2_b32 v[178:179], v146 offset0:77 offset1:93
	ds_read2_b32 v[180:181], v146 offset0:142 offset1:158
	s_waitcnt lgkmcnt(3)
	v_mul_f32_e32 v153, 0x42000000, v174
	v_med3_f32 v2, v153, s41, v143
	ds_read2_b32 v[182:183], v146 offset0:207 offset1:223
	v_cvt_pk_fp8_f32 v152, v0, v2 op_sel:[0,0,1]
	s_waitcnt lgkmcnt(3)
	v_mul_f32_e32 v0, 0x42000000, v176
	s_waitcnt lgkmcnt(2)
	v_mul_f32_e32 v2, 0x42000000, v178
	v_med3_f32 v0, v0, s41, v143
	v_med3_f32 v2, v2, s41, v143
	v_mov_b32_e32 v153, 0
	v_cvt_pk_fp8_f32 v153, v0, v2
	s_waitcnt lgkmcnt(1)
	v_mul_f32_e32 v154, 0x42000000, v180
	s_waitcnt lgkmcnt(0)
; #define GAS __attribute__((address_space(1)))
; __device__ __forceinline__ unsigned pk_fp8x4(float a, float b, float c, float d) { int p = __builtin_amdgcn_cvt_pk_fp8_f32(sat8(a), sat8(b), 0, false); p = __builtin_amdgcn_cvt_pk_fp8_f32(sat8(c), sat8(d), p, true); return (unsigned)p; }
; __device__ __forceinline__ void tr_finish(const TrDesc& d, f32x4 (&v)[16], LAS float* scr, int lane) {
;     ...
;         for (int j = 0; j < 4; ++j) { u32x4 o;
;             o.x = pk_fp8x4(sp[0 * 65 + 16 * j] * 32.0f, sp[1 * 65 + 16 * j] * 32.0f, sp[2 * 65 + 16 * j] * 32.0f, sp[3 * 65 + 16 * j] * 32.0f);
;             o.y = pk_fp8x4(sp[4 * 65 + 16 * j] * 32.0f, sp[5 * 65 + 16 * j] * 32.0f, sp[6 * 65 + 16 * j] * 32.0f, sp[7 * 65 + 16 * j] * 32.0f);
;             o.z = pk_fp8x4(sp[8 * 65 + 16 * j] * 32.0f, sp[9 * 65 + 16 * j] * 32.0f, sp[10 * 65 + 16 * j] * 32.0f, sp[11 * 65 + 16 * j] * 32.0f);
;             o.w = pk_fp8x4(sp[12 * 65 + 16 * j] * 32.0f, sp[13 * 65 + 16 * j] * 32.0f, sp[14 * 65 + 16 * j] * 32.0f, sp[15 * 65 + 16 * j] * 32.0f);
;             *(GAS u32x4*)(dp + (size_t)(16 * j) * d.K) = o; }
;     ...
;             if (itB >= NIT) break;
;             const int itA = itB + NGW;
;             if (itA < NIT) { dA = decode(NIT - 1 - itA); tr_load(dA, vA); }
	v_mul_f32_e32 v0, 0x42000000, v182
	v_med3_f32 v2, v154, s41, v143
	v_med3_f32 v0, v0, s41, v143
	v_cvt_pk_fp8_f32 v153, v2, v0 op_sel:[0,0,1]
	v_mov_b64_e32 v[158:159], s[16:17]
	v_mad_i64_i32 v[158:159], s[22:23], s2, v132, v[158:159]
	v_lshl_add_u64 v[158:159], v[158:159], 0, v[134:135]
	v_mul_f32_e32 v0, 0x42000000, v3
	v_mul_f32_e32 v2, 0x42000000, v149
	global_store_dwordx4 v[158:159], v[150:153], off
	v_med3_f32 v0, v0, s41, v143
	v_med3_f32 v2, v2, s41, v143
	v_mov_b32_e32 v150, 0
	v_cvt_pk_fp8_f32 v150, v0, v2
	v_mul_f32_e32 v3, 0x42000000, v155
	v_mul_f32_e32 v0, 0x42000000, v157
	v_med3_f32 v2, v3, s41, v143
	v_med3_f32 v0, v0, s41, v143
	v_cvt_pk_fp8_f32 v150, v2, v0 op_sel:[0,0,1]
	v_mul_f32_e32 v0, 0x42000000, v161
	v_mul_f32_e32 v2, 0x42000000, v163
	v_med3_f32 v0, v0, s41, v143
	v_med3_f32 v2, v2, s41, v143
	v_mov_b32_e32 v151, 0
	v_cvt_pk_fp8_f32 v151, v0, v2
	v_mul_f32_e32 v3, 0x42000000, v165
	v_mul_f32_e32 v0, 0x42000000, v167
	v_med3_f32 v2, v3, s41, v143
	v_med3_f32 v0, v0, s41, v143
	v_cvt_pk_fp8_f32 v151, v2, v0 op_sel:[0,0,1]
	v_mul_f32_e32 v0, 0x42000000, v169
	v_mul_f32_e32 v2, 0x42000000, v171
	v_med3_f32 v0, v0, s41, v143
	v_med3_f32 v2, v2, s41, v143
	v_mov_b32_e32 v152, 0
	v_cvt_pk_fp8_f32 v152, v0, v2
	v_mul_f32_e32 v3, 0x42000000, v173
	v_mul_f32_e32 v0, 0x42000000, v175
	v_med3_f32 v2, v3, s41, v143
	v_med3_f32 v0, v0, s41, v143
	v_cvt_pk_fp8_f32 v152, v2, v0 op_sel:[0,0,1]
	v_mul_f32_e32 v0, 0x42000000, v177
	v_mul_f32_e32 v2, 0x42000000, v179
	v_med3_f32 v0, v0, s41, v143
	v_med3_f32 v2, v2, s41, v143
	v_mov_b32_e32 v153, 0
	v_cvt_pk_fp8_f32 v153, v0, v2
	s_ashr_i32 s3, s2, 31
	v_mul_f32_e32 v3, 0x42000000, v181
	v_mul_f32_e32 v0, 0x42000000, v183
	v_med3_f32 v2, v3, s41, v143
	v_med3_f32 v0, v0, s41, v143
	s_lshl_b64 s[22:23], s[2:3], 4
	v_cvt_pk_fp8_f32 v153, v2, v0 op_sel:[0,0,1]
	v_lshl_add_u64 v[2:3], v[158:159], 0, s[22:23]
	ds_read2_b32 v[154:155], v142 offset0:32 offset1:48
	ds_read2_b32 v[156:157], v142 offset0:97 offset1:113
	ds_read2_b32 v[158:159], v142 offset0:162 offset1:178
	ds_read2_b32 v[160:161], v142 offset0:227 offset1:243
	s_andn2_b64 vcc, exec, s[20:21]
	s_waitcnt lgkmcnt(3)
	v_mul_f32_e32 v0, 0x42000000, v154
	s_waitcnt lgkmcnt(2)
	v_mul_f32_e32 v149, 0x42000000, v156
	global_store_dwordx4 v[2:3], v[150:153], off
	v_med3_f32 v0, v0, s41, v143
	v_med3_f32 v149, v149, s41, v143
	v_mov_b32_e32 v150, 0
	v_cvt_pk_fp8_f32 v150, v0, v149
	ds_read2_b32 v[162:163], v147 offset0:36 offset1:52
	ds_read2_b32 v[164:165], v147 offset0:101 offset1:117
	ds_read2_b32 v[166:167], v147 offset0:166 offset1:182
	ds_read2_b32 v[168:169], v147 offset0:231 offset1:247
	s_waitcnt lgkmcnt(5)
	v_mul_f32_e32 v151, 0x42000000, v158
	s_waitcnt lgkmcnt(4)
	v_mul_f32_e32 v152, 0x42000000, v160
	v_med3_f32 v0, v151, s41, v143
	v_med3_f32 v149, v152, s41, v143
	v_cvt_pk_fp8_f32 v150, v0, v149 op_sel:[0,0,1]
	s_waitcnt lgkmcnt(3)
	v_mul_f32_e32 v0, 0x42000000, v162
	s_waitcnt lgkmcnt(2)
	v_mul_f32_e32 v149, 0x42000000, v164
	v_med3_f32 v0, v0, s41, v143
	v_med3_f32 v149, v149, s41, v143
	v_mov_b32_e32 v151, 0
	v_cvt_pk_fp8_f32 v151, v0, v149
	ds_read2_b32 v[170:171], v148 offset0:40 offset1:56
	ds_read2_b32 v[172:173], v148 offset0:105 offset1:121
	ds_read2_b32 v[174:175], v148 offset0:170 offset1:186
	ds_read2_b32 v[176:177], v148 offset0:235 offset1:251
	s_waitcnt lgkmcnt(5)
	v_mul_f32_e32 v152, 0x42000000, v166
	s_waitcnt lgkmcnt(4)
	v_mul_f32_e32 v153, 0x42000000, v168
	v_med3_f32 v0, v152, s41, v143
	v_med3_f32 v149, v153, s41, v143
	v_cvt_pk_fp8_f32 v151, v0, v149 op_sel:[0,0,1]
	s_waitcnt lgkmcnt(3)
	v_mul_f32_e32 v0, 0x42000000, v170
	s_waitcnt lgkmcnt(2)
	v_mul_f32_e32 v149, 0x42000000, v172
	v_med3_f32 v0, v0, s41, v143
	v_med3_f32 v149, v149, s41, v143
	v_mov_b32_e32 v152, 0
	v_cvt_pk_fp8_f32 v152, v0, v149
	ds_read2_b32 v[178:179], v146 offset0:44 offset1:60
	ds_read2_b32 v[180:181], v146 offset0:109 offset1:125
	ds_read2_b32 v[182:183], v146 offset0:174 offset1:190
	s_waitcnt lgkmcnt(4)
	v_mul_f32_e32 v153, 0x42000000, v174
	s_waitcnt lgkmcnt(3)
	v_mul_f32_e32 v154, 0x42000000, v176
	v_med3_f32 v0, v153, s41, v143
	v_med3_f32 v149, v154, s41, v143
	ds_read2_b32 v[184:185], v146 offset0:239 offset1:255
	v_cvt_pk_fp8_f32 v152, v0, v149 op_sel:[0,0,1]
	s_waitcnt lgkmcnt(3)
	v_mul_f32_e32 v0, 0x42000000, v178
	s_waitcnt lgkmcnt(2)
	v_mul_f32_e32 v149, 0x42000000, v180
	v_med3_f32 v0, v0, s41, v143
	v_med3_f32 v149, v149, s41, v143
	v_mov_b32_e32 v153, 0
	v_cvt_pk_fp8_f32 v153, v0, v149
	s_waitcnt lgkmcnt(1)
	v_mul_f32_e32 v154, 0x42000000, v182
	s_waitcnt lgkmcnt(0)
	v_mul_f32_e32 v0, 0x42000000, v184
	v_med3_f32 v149, v154, s41, v143
	v_med3_f32 v0, v0, s41, v143
	v_cvt_pk_fp8_f32 v153, v149, v0 op_sel:[0,0,1]
	v_mul_f32_e32 v0, 0x42000000, v155
	v_mul_f32_e32 v149, 0x42000000, v157
	v_med3_f32 v0, v0, s41, v143
	v_med3_f32 v149, v149, s41, v143
	v_mov_b32_e32 v154, 0
	v_cvt_pk_fp8_f32 v154, v0, v149
	v_mul_f32_e32 v155, 0x42000000, v159
	v_mul_f32_e32 v0, 0x42000000, v161
	v_med3_f32 v149, v155, s41, v143
	v_med3_f32 v0, v0, s41, v143
	v_cvt_pk_fp8_f32 v154, v149, v0 op_sel:[0,0,1]
	v_mul_f32_e32 v0, 0x42000000, v163
	v_mul_f32_e32 v149, 0x42000000, v165
	v_med3_f32 v0, v0, s41, v143
	v_med3_f32 v149, v149, s41, v143
	v_mov_b32_e32 v155, 0
	v_cvt_pk_fp8_f32 v155, v0, v149
	v_mul_f32_e32 v156, 0x42000000, v167
	v_mul_f32_e32 v0, 0x42000000, v169
	v_med3_f32 v149, v156, s41, v143
	v_med3_f32 v0, v0, s41, v143
	v_cvt_pk_fp8_f32 v155, v149, v0 op_sel:[0,0,1]
	v_mul_f32_e32 v0, 0x42000000, v171
	v_mul_f32_e32 v149, 0x42000000, v173
	v_med3_f32 v0, v0, s41, v143
	v_med3_f32 v149, v149, s41, v143
	v_mov_b32_e32 v156, 0
	v_cvt_pk_fp8_f32 v156, v0, v149
	v_mul_f32_e32 v157, 0x42000000, v175
	v_mul_f32_e32 v0, 0x42000000, v177
	v_med3_f32 v149, v157, s41, v143
	v_med3_f32 v0, v0, s41, v143
	v_cvt_pk_fp8_f32 v156, v149, v0 op_sel:[0,0,1]
	v_mul_f32_e32 v0, 0x42000000, v179
	v_mul_f32_e32 v149, 0x42000000, v181
	v_med3_f32 v0, v0, s41, v143
	v_med3_f32 v149, v149, s41, v143
	v_mov_b32_e32 v157, 0
	v_cvt_pk_fp8_f32 v157, v0, v149
	v_mul_f32_e32 v158, 0x42000000, v183
	v_mul_f32_e32 v0, 0x42000000, v185
	v_med3_f32 v149, v158, s41, v143
	v_med3_f32 v0, v0, s41, v143
	v_cvt_pk_fp8_f32 v157, v149, v0 op_sel:[0,0,1]
	v_lshl_add_u64 v[2:3], v[2:3], 0, s[22:23]
	global_store_dwordx4 v[2:3], v[150:153], off
	v_lshl_add_u64 v[2:3], v[2:3], 0, s[22:23]
	global_store_dwordx4 v[2:3], v[154:157], off
	s_waitcnt lgkmcnt(0)
	s_cbranch_vccnz .LBB0_71_hp
	s_bitcmp1_b32 s44, 5
	s_cbranch_scc1 .Ladv42_else_hp
	s_add_i32 s42, s44, 32
	s_branch .Ladv42_end_hp
;     ...
;         auto decode = [&](int it) -> TrDesc {
;             TrDesc d; d.zero = 0; d.rope = 0; d.f8 = 0;
;             const int l = it / C_L; int r = it % C_L;
;             const float* W; unsigned char* WT; int ldw, K, k0, n0, scol, esz = 2;
;             if (r < C_IN) { const int kb = r / 188, nb = r % 188; n0 = 64 * nb; k0 = 64 * kb; ldw = NIN; K = D; W = a.w_in + (size_t)l * D * NIN;
;                 if (n0 < 3072) { d.rope = 1; scol = (n0 >> 7) * 128 + 32 * ((n0 >> 6) & 1) + 64 * (q4 >> 3) + 4 * (q4 & 7); }
;                 else if (n0 < 7680) scol = n0 + 4 * q4;
;                 else if (n0 < 11776) scol = n0 + 16 + 4 * q4;
;                 else if (n0 == 11776) { scol = (q4 < 4) ? 7680 + 4 * q4 : 0; d.zero = (q4 < 4) ? 0 : 1; }
;                 else { scol = 0; d.zero = 1; }
;     ...
;                 d.f8 = 1; esz = 1; WT = ws + WS_WIN + (size_t)l * NP * D;
;     ...
;                 WT = ws + WS_WIN + (size_t)l * NP * D * 2;
;     ...
;             } else if ((r -= C_IN) < C_OA) { const int kb = r / 32, nb = r % 32; n0 = 64 * nb; k0 = 64 * kb; ldw = D; K = 512; scol = n0 + 4 * q4; W = a.w_out_a + (size_t)l * 512 * D; WT = ws + WS_WOA + (size_t)l * D * 512 * (MIX_F8 ? 1 : 2); if (MIX_F8) { d.f8 = 1; esz = 1; }
;                 if (BR_FUSE) { K = 1536; WT = ws + WS_WOA + (size_t)l * D * 1536 + 1024; }
;             } else if ((r -= C_OA) < C_OB) { const int kb = r / 32, nb = r % 32; n0 = 64 * nb; k0 = 64 * kb; ldw = D; K = 1024; scol = n0 + 4 * q4; W = a.w_out_b + (size_t)l * 1024 * D; WT = ws + WS_WOB + (size_t)l * D * 1024 * (MIX_F8 ? 1 : 2); if (MIX_F8) { d.f8 = 1; esz = 1; }
;                 if (BR_FUSE) { K = 1536; WT = ws + WS_WOA + (size_t)l * D * 1536; }
;             } else if ((r -= C_OB) < C_O) { const int kb = r / 32, nb = r % 32; n0 = 64 * nb; k0 = 64 * kb; ldw = D; K = D; scol = n0 + 4 * q4; W = a.w_out + (size_t)l * D * D; WT = ws + WS_WO + (size_t)l * D * D * (MIX_F8 ? 1 : 2); if (MIX_F8) { d.f8 = 1; esz = 1; }
;             } else if ((r -= C_O) < C_GU) { const int e = r / 1024, r2 = r % 1024, kb = r2 / 32, nb = r2 % 32, pn = nb >> 2, sgu = (nb >> 1) & 1, c0 = 64 * (nb & 1);
;                 n0 = 64 * nb; k0 = 64 * kb; ldw = FF; K = D; scol = 128 * pn + c0 + 4 * q4; W = (sgu ? a.w_up_e : a.w_gate_e) + (size_t)(l * NE + e) * D * FF; WT = ws + WS_WGU + (size_t)(l * NE + e) * 2048 * D; d.f8 = 1; esz = 1;
.Ladv42_else_hp:
	s_lshr_b32 s42, s44, 6
	s_lshl_b32 s42, s42, 2
	s_bfe_u32 s100, s44, 0x20003
	s_or_b32 s42, s42, s100
	s_add_i32 s42, s42, s74
	s_and_b32 s100, s42, 3
	s_lshr_b32 s42, s42, 2
	s_lshl_b32 s42, s42, 6
	s_lshl_b32 s100, s100, 3
	s_or_b32 s42, s42, s100
	s_and_b32 s100, s44, 7
	s_or_b32 s42, s42, s100
.Ladv42_end_hp:
	s_cmp_ge_i32 s42, s101
	s_cbranch_scc1 .LBB0_144_hp
	s_sub_i32 s2, 0xfcff, s42
	s_mul_hi_u32 s0, s2, 0x81848da9
	s_lshr_b32 s0, s0, 14
	s_mul_i32 s3, s0, 0x7e80
	s_sub_i32 s27, s2, s3
	s_cmpk_gt_u32 s27, 0x177f
	s_cbranch_scc0 .LBB0_117_hp
	s_cmpk_gt_u32 s27, 0x187f
	s_cbranch_scc0 .LBB0_119_hp
	s_cmpk_gt_u32 s27, 0x1a7f
	s_cbranch_scc0 .LBB0_120_hp
	s_cmpk_gt_u32 s27, 0x1e7f
	s_cbranch_scc0 .LBB0_123_hp
	s_lshl_b32 s22, s27, 6
	s_cmpk_gt_u32 s27, 0x5e7f
	s_cbranch_scc0 .LBB0_147_hp
	s_add_i32 s2, s27, 0xffffa180
	s_lshr_b32 s16, s2, 9
	s_lshl_b32 s2, s2, 1
	s_and_b32 s44, s2, 0x3c0
	s_load_dwordx2 s[2:3], s[8:9], 0x88
	s_lshl_b32 s17, s0, 4
	s_add_i32 s20, s16, s17
	s_mov_b32 s21, s1
	s_and_b32 s15, s22, 0x7c0
	s_lshl_b64 s[16:17], s[20:21], 23
	s_waitcnt lgkmcnt(0)
	s_add_u32 s16, s2, s16
	s_addc_u32 s17, s3, s17
	s_lshl_b64 s[2:3], s[20:21], 21
	s_add_u32 s20, s28, s2
	v_or_b32_e32 v0, s15, v136
	s_addc_u32 s21, s29, s3
	s_cbranch_execz .LBB0_148_hp
	s_movk_i32 s2, 0x400
	s_mov_b64 s[22:23], 0x800
	s_cbranch_execz .LBB0_124_hp
	s_branch .LBB0_125_hp

; #define LAS __attribute__((address_space(3)))
; #define FRESH_TID() do { ap = fresh_args(); ws = ap->ws; unsigned m1_ = ~0u; asm volatile("" : "+s"(m1_)); lane = (int)__builtin_amdgcn_mbcnt_hi(m1_, __builtin_amdgcn_mbcnt_lo(m1_, 0u)); asm volatile("" : "+v"(lane)); wave = wave0; tid = wave0 * 64 + lane; } while (0)
; __device__ __forceinline__ void moe_table_build(LAS unsigned char* lds, const unsigned* cnt, int tid) {
;     ...
;     __syncthreads();
;     if (tid == 0) { int acc = 0; for (int e = 0; e < NE; ++e) { acc += (((LAS int*)(lds + MOE_TAB_OFF))[16 + e] + 255) >> 8; ((LAS int*)(lds + MOE_TAB_OFF))[e] = acc; } }
;     __syncthreads();
; }
;     __device__ __forceinline__ void init(LAS unsigned char* lds_, int nN_, int G_, int c_) {
;         lds = lds_; NT = __builtin_amdgcn_readfirstlane(((LAS int*)(lds + MOE_TAB_OFF))[15]); nN = nN_; G = G_; c = c_; }
; template <unsigned MASK, bool ONE>
; __global__ void __launch_bounds__(NTHREADS, 2) fwd_kernel(Args a_unused) {
;     ...
;         if (IN(P + 9, 10)) { FRESH_TID();
;             pg8::moe_table_build(lds, cntl, tid);
;             pg8::MoeOrder S; S.init(lds, 8, G, bx); pg8::RowsContig AM; pg8::EpiPlainS E{Y, pg8::W8_INV};
.LBB0_1010:
	s_or_b64 exec, exec, s[0:1]
	v_readlane_b32 s0, v254, 58
	s_waitcnt lgkmcnt(0)
	s_barrier
	v_mov_b32_e32 v2, s0
	ds_read_b32 v2, v2
	v_readlane_b32 s1, v253, 4
	v_readfirstlane_b32 s14, v1
	v_readlane_b32 s65, v255, 22
	s_movk_i32 s66, 0x179
	s_waitcnt lgkmcnt(0)
	v_readfirstlane_b32 s16, v2
	s_lshl_b32 s0, s16, 3
	s_cmp_eq_u32 s101, 0
	s_cbranch_scc1 .Lno_help10
	s_cmpk_lt_i32 s1, 0xc0
	s_cbranch_scc1 .Lno_help10
	s_mov_b32 s100, 0x1ac0
	s_mov_b32 s101, 0x3cc0
	s_mov_b32 s62, 0x20600000
	s_mov_b32 s0, 1
	v_writelane_b32 v251, s0, 30
	s_movk_i32 s0, 64
	s_branch .Lhp_entry
